# p7 pass loop: the next pass's row prefetch is no longer forced to land by a mid-pass full wait (rare modulation-vector block retires its own loads; prefetch waited for before the pass's second barrier
# baseline (speedup 1.0000x reference)
; __device__ __forceinline__ float bflo(unsigned w) { return __uint_as_float(w << 16); }
; __device__ __forceinline__ float bfhi(unsigned w) { return __uint_as_float(w & 0xffff0000u); }
; #define P7_PRELOAD(r) do { const int ra_ = ((r) < nrows) ? (r) : 0; const bf16_t* sa_ = xb + (size_t)ra_ * D; const bf16_t* sb_ = sa_ + D; \
;         _Pragma("unroll") for (int j = 0; j < 4; ++j) { nva[j] = *(const u32x2*)(sa_ + 4 * (lane + 64 * j)); nvb[j] = *(const u32x2*)(sb_ + 4 * (lane + 64 * j)); } } while (0)
; __device__ __forceinline__ void p7_norm2(const Frame& F, int layer) {
;     ...
;     for (int pi = 0; pi < RW / 2; ++pi) {
;         const int row0 = rbeg + 2 * pi; const bool vR = row0 < nrows; const int rowA = vR ? row0 : 0, rowB = rowA + 1;
;         const int mR = (rowA < NL) ? (rowA >> 11) : 16;
;         f32x4 va[4], vb[4]; float sa = 0.f, sb = 0.f;
; #pragma unroll
;         for (int j = 0; j < 4; ++j) { va[j] = (f32x4){bflo(nva[j].x), bfhi(nva[j].x), bflo(nva[j].y), bfhi(nva[j].y)}; vb[j] = (f32x4){bflo(nvb[j].x), bfhi(nvb[j].x), bflo(nvb[j].y), bfhi(nvb[j].y)};
;             sa += va[j][0] * va[j][0] + va[j][1] * va[j][1] + va[j][2] * va[j][2] + va[j][3] * va[j][3];
;             sb += vb[j][0] * vb[j][0] + vb[j][1] * vb[j][1] + vb[j][2] * vb[j][2] + vb[j][3] * vb[j][3]; }
;         if (pi + 1 < RW / 2) P7_PRELOAD(row0 + 2);
;         if (mR != cur_m) { cur_m = mR; const float* sh = modl + mR * 6144 + 3 * 1024; const float* sc = sh + 1024;
; #pragma unroll
;             for (int j = 0; j < 4; ++j) { const int k = 4 * (lane + 64 * j); W1[j] = *(const f32x4*)(n2w + k) * (*(const f32x4*)(sc + k) + 1.f); S0[j] = *(const f32x4*)(sh + k); } }
;         sa = wave_sum_dpp(sa); sb = wave_sum_dpp(sb);
.LBB0_831:
	s_cmp_lt_i32 s2, s18
	s_cselect_b64 s[10:11], -1, 0
	s_and_b64 s[12:13], s[10:11], exec
	s_cselect_b32 s3, s2, 0
	s_min_i32 s12, s3, 0x8000
	s_ashr_i32 s36, s12, 11
	s_cmp_eq_u32 s36, s14
	s_cbranch_scc1 .LBB0_833
	s_mul_i32 s12, s36, 0x1800
	s_ashr_i32 s13, s12, 31
	s_lshl_b64 s[12:13], s[12:13], 2
	s_add_u32 s14, s20, s12
	s_addc_u32 s15, s21, s13
	s_add_u32 s12, s14, 0x203000
	s_addc_u32 s13, s15, 0
	s_add_u32 s14, s14, 0x204000
	s_addc_u32 s15, s15, 0
	v_lshl_add_u64 v[4:5], s[14:15], 0, v[32:33]
	v_lshl_add_u64 v[12:13], s[14:15], 0, v[36:37]
	v_lshl_add_u64 v[20:21], s[14:15], 0, v[38:39]
	v_lshl_add_u64 v[28:29], s[14:15], 0, v[40:41]
	global_load_dwordx4 v[4:7], v[4:5], off
	s_nop 0
	global_load_dwordx4 v[12:15], v[12:13], off
	s_nop 0
	global_load_dwordx4 v[20:23], v[20:21], off
	s_nop 0
	global_load_dwordx4 v[28:31], v[28:29], off
	s_nop 0
	global_load_dwordx4 v[0:3], v[44:45], off
	s_nop 0
	global_load_dwordx4 v[8:11], v[44:45], off offset:1024
	s_nop 0
	global_load_dwordx4 v[16:19], v[44:45], off offset:2048
	s_nop 0
	global_load_dwordx4 v[24:27], v[44:45], off offset:3072
	s_mov_b32 s14, s36
	s_waitcnt vmcnt(0)
	v_pk_add_f32 v[4:5], v[4:5], 1.0 op_sel_hi:[1,0]
	v_pk_add_f32 v[6:7], v[6:7], 1.0 op_sel_hi:[1,0]
	v_pk_add_f32 v[12:13], v[12:13], 1.0 op_sel_hi:[1,0]
	v_pk_add_f32 v[14:15], v[14:15], 1.0 op_sel_hi:[1,0]
	v_pk_add_f32 v[20:21], v[20:21], 1.0 op_sel_hi:[1,0]
	v_pk_add_f32 v[22:23], v[22:23], 1.0 op_sel_hi:[1,0]
	v_pk_add_f32 v[28:29], v[28:29], 1.0 op_sel_hi:[1,0]
	v_pk_add_f32 v[30:31], v[30:31], 1.0 op_sel_hi:[1,0]
	v_pk_mul_f32 v[0:1], v[0:1], v[4:5]
	v_pk_mul_f32 v[2:3], v[2:3], v[6:7]
	v_pk_mul_f32 v[8:9], v[8:9], v[12:13]
	v_pk_mul_f32 v[10:11], v[10:11], v[14:15]
	v_pk_mul_f32 v[16:17], v[16:17], v[20:21]
	v_pk_mul_f32 v[18:19], v[18:19], v[22:23]
	v_pk_mul_f32 v[24:25], v[24:25], v[28:29]
	v_pk_mul_f32 v[26:27], v[26:27], v[30:31]
	v_lshl_add_u64 v[4:5], s[12:13], 0, v[32:33]
	v_lshl_add_u64 v[12:13], s[12:13], 0, v[36:37]
	v_lshl_add_u64 v[20:21], s[12:13], 0, v[38:39]
	v_lshl_add_u64 v[28:29], s[12:13], 0, v[40:41]
	global_load_dwordx4 v[4:7], v[4:5], off
	s_nop 0
	global_load_dwordx4 v[12:15], v[12:13], off
	s_nop 0
	global_load_dwordx4 v[20:23], v[20:21], off
	s_nop 0
	global_load_dwordx4 v[28:31], v[28:29], off
	s_waitcnt vmcnt(0)
.LBB0_833:
	v_and_b32_e32 v79, 0xffff0000, v74
	v_and_b32_e32 v85, 0xffff0000, v70
	v_lshlrev_b32_e32 v78, 16, v74
	v_mul_f32_e32 v82, v79, v79
	v_lshlrev_b32_e32 v84, 16, v70
	v_mul_f32_e32 v86, v85, v85
	v_lshlrev_b32_e32 v74, 16, v75
	v_fmac_f32_e32 v82, v78, v78
	v_lshlrev_b32_e32 v70, 16, v71
	v_fmac_f32_e32 v86, v84, v84
	v_and_b32_e32 v75, 0xffff0000, v75
	v_fmac_f32_e32 v82, v74, v74
	v_and_b32_e32 v71, 0xffff0000, v71
	v_fmac_f32_e32 v86, v70, v70
	v_and_b32_e32 v81, 0xffff0000, v76
	v_fmac_f32_e32 v82, v75, v75
	v_and_b32_e32 v89, 0xffff0000, v72
	v_fmac_f32_e32 v86, v71, v71
	v_and_b32_e32 v91, 0xffff0000, v66
	v_lshlrev_b32_e32 v80, 16, v76
	v_mul_f32_e32 v83, v81, v81
	v_lshlrev_b32_e32 v88, 16, v72
	v_add_f32_e32 v82, v86, v82
	v_mul_f32_e32 v86, v89, v89
	v_lshlrev_b32_e32 v90, 16, v66
	v_and_b32_e32 v109, 0xffff0000, v68
	v_mul_f32_e32 v66, v91, v91
	v_and_b32_e32 v111, 0xffff0000, v62
	v_lshlrev_b32_e32 v76, 16, v77
	v_fmac_f32_e32 v83, v80, v80
	v_lshlrev_b32_e32 v72, 16, v73
	v_fmac_f32_e32 v86, v88, v88
	v_lshlrev_b32_e32 v92, 16, v67
	v_and_b32_e32 v93, 0xffff0000, v67
	v_lshlrev_b32_e32 v108, 16, v68
	v_fmac_f32_e32 v66, v90, v90
	v_mul_f32_e32 v67, v109, v109
	v_lshlrev_b32_e32 v110, 16, v62
	v_and_b32_e32 v115, 0xffff0000, v64
	v_mul_f32_e32 v62, v111, v111
	v_and_b32_e32 v77, 0xffff0000, v77
	v_fmac_f32_e32 v83, v76, v76
	v_and_b32_e32 v73, 0xffff0000, v73
	v_fmac_f32_e32 v86, v72, v72
	v_lshlrev_b32_e32 v68, 16, v69
	v_fmac_f32_e32 v66, v92, v92
	v_fmac_f32_e32 v67, v108, v108
	v_lshlrev_b32_e32 v112, 16, v63
	v_and_b32_e32 v113, 0xffff0000, v63
	v_lshlrev_b32_e32 v114, 16, v64
	v_fmac_f32_e32 v62, v110, v110
	v_mul_f32_e32 v63, v115, v115
	v_fmac_f32_e32 v83, v77, v77
	v_fmac_f32_e32 v86, v73, v73
	v_and_b32_e32 v69, 0xffff0000, v69
	v_fmac_f32_e32 v66, v93, v93
	v_fmac_f32_e32 v67, v68, v68
	v_lshlrev_b32_e32 v116, 16, v65
	v_fmac_f32_e32 v62, v112, v112
	v_fmac_f32_e32 v63, v114, v114
	v_add_f32_e32 v83, v86, v83
	v_add_f32_e32 v66, v66, v82
	v_fmac_f32_e32 v67, v69, v69
	v_and_b32_e32 v117, 0xffff0000, v65
	v_fmac_f32_e32 v62, v113, v113
	v_fmac_f32_e32 v63, v116, v116
	v_add_f32_e32 v67, v67, v83
	v_add_f32_e32 v62, v62, v66
	v_fmac_f32_e32 v63, v117, v117
	v_add_f32_e32 v64, v63, v67
	v_add_f32_dpp v62, v62, v62 quad_perm:[1,0,3,2] row_mask:0xf bank_mask:0xf bound_ctrl:1
	s_nop 0
	v_add_f32_dpp v64, v64, v64 quad_perm:[1,0,3,2] row_mask:0xf bank_mask:0xf bound_ctrl:1
	v_add_f32_dpp v62, v62, v62 quad_perm:[2,3,0,1] row_mask:0xf bank_mask:0xf bound_ctrl:1
	s_nop 0
	v_add_f32_dpp v64, v64, v64 quad_perm:[2,3,0,1] row_mask:0xf bank_mask:0xf bound_ctrl:1
	v_add_f32_dpp v62, v62, v62 row_half_mirror row_mask:0xf bank_mask:0xf bound_ctrl:1
	s_nop 0
	v_add_f32_dpp v64, v64, v64 row_half_mirror row_mask:0xf bank_mask:0xf bound_ctrl:1
	v_add_f32_dpp v62, v62, v62 row_mirror row_mask:0xf bank_mask:0xf bound_ctrl:1
	s_nop 0
	v_readlane_b32 s15, v62, 16
	v_readlane_b32 s36, v62, 48
	v_add_f32_dpp v64, v64, v64 row_mirror row_mask:0xf bank_mask:0xf bound_ctrl:1
	v_readlane_b32 s12, v62, 0
	v_readlane_b32 s13, v62, 32
	v_mov_b32_e32 v62, s15
	v_mov_b32_e32 v63, s36
	v_readlane_b32 s15, v64, 16
	v_readlane_b32 s36, v64, 48
	v_pk_add_f32 v[62:63], s[12:13], v[62:63]
	v_readlane_b32 s12, v64, 0
	v_readlane_b32 s13, v64, 32
	v_mov_b32_e32 v64, s15
; __device__ __forceinline__ void p7_norm2(const Frame& F, int layer) {
;     ...
;         sa = wave_sum_dpp(sa); sb = wave_sum_dpp(sb);
;         float ma = 0.f, mb = 0.f;
;         { const float rsa = rsqrtf(sa * (1.f / D) + EPS), rsb = rsqrtf(sb * (1.f / D) + EPS);
; #pragma unroll
;           for (int j = 0; j < 4; ++j) {
;               const f32x4 ha = va[j] * rsa * W1[j] + S0[j], hb = vb[j] * rsb * W1[j] + S0[j];
;               ma = fmaxf(fmaxf(ma, fmaxf(fabsf(ha[0]), fabsf(ha[1]))), fmaxf(fabsf(ha[2]), fabsf(ha[3])));
;               mb = fmaxf(fmaxf(mb, fmaxf(fabsf(hb[0]), fabsf(hb[1]))), fmaxf(fabsf(hb[2]), fabsf(hb[3])));
;               va[j] = ha; vb[j] = hb; } }
;         ma = wave_max_dpp(ma); mb = wave_max_dpp(mb);
	v_mov_b32_e32 v65, s36
	v_pk_add_f32 v[64:65], s[12:13], v[64:65]
	v_mov_b32_e32 v67, v62
	v_mov_b32_e32 v66, v64
	v_mov_b32_e32 v62, v65
	v_pk_add_f32 v[62:63], v[66:67], v[62:63]
	s_nop 0
	v_pk_fma_f32 v[62:63], v[62:63], s[86:87], v[246:247] op_sel_hi:[1,0,0]
	s_nop 0
	v_mul_f32_e32 v64, 0x4b800000, v63
	v_cmp_gt_f32_e32 vcc, s22, v63
	v_cmp_gt_f32_e64 s[40:41], s22, v62
	s_nop 0
	v_cndmask_b32_e32 v63, v63, v64, vcc
	v_mul_f32_e32 v64, 0x4b800000, v62
	v_rsq_f32_e32 v63, v63
	v_cndmask_b32_e64 v62, v62, v64, s[40:41]
	v_rsq_f32_e32 v62, v62
	v_mul_f32_e32 v64, 0x45800000, v63
	v_cndmask_b32_e32 v118, v63, v64, vcc
	v_mul_f32_e32 v63, 0x45800000, v62
	v_cndmask_b32_e64 v120, v62, v63, s[40:41]
	v_pk_mul_f32 v[62:63], v[78:79], v[118:119] op_sel_hi:[1,0]
	v_pk_mul_f32 v[64:65], v[74:75], v[118:119] op_sel_hi:[1,0]
	v_pk_fma_f32 v[82:83], v[0:1], v[62:63], v[4:5]
	v_pk_fma_f32 v[78:79], v[2:3], v[64:65], v[6:7]
	v_pk_mul_f32 v[64:65], v[80:81], v[120:121] op_sel_hi:[1,0]
	v_pk_mul_f32 v[62:63], v[76:77], v[120:121] op_sel_hi:[1,0]
	v_pk_fma_f32 v[66:67], v[0:1], v[64:65], v[4:5]
	v_pk_fma_f32 v[62:63], v[2:3], v[62:63], v[6:7]
	v_max_f32_e64 v64, |v82|, |v83|
	v_max_f32_e64 v65, |v78|, |v79|
	v_max3_f32 v74, v64, 0, v65
	v_max_f32_e64 v64, |v66|, |v67|
	v_max_f32_e64 v65, |v62|, |v63|
	v_max3_f32 v75, v64, 0, v65
	v_pk_mul_f32 v[64:65], v[84:85], v[118:119] op_sel_hi:[1,0]
	v_pk_mul_f32 v[70:71], v[70:71], v[118:119] op_sel_hi:[1,0]
	v_pk_fma_f32 v[86:87], v[8:9], v[64:65], v[12:13]
	v_pk_fma_f32 v[80:81], v[10:11], v[70:71], v[14:15]
	v_pk_mul_f32 v[70:71], v[88:89], v[120:121] op_sel_hi:[1,0]
	v_pk_mul_f32 v[64:65], v[72:73], v[120:121] op_sel_hi:[1,0]
	v_pk_fma_f32 v[70:71], v[8:9], v[70:71], v[12:13]
	v_pk_fma_f32 v[64:65], v[10:11], v[64:65], v[14:15]
	v_max_f32_e64 v72, |v86|, |v87|
	v_max_f32_e64 v73, |v80|, |v81|
	v_max3_f32 v76, v74, v72, v73
	v_max_f32_e64 v72, |v70|, |v71|
	v_max_f32_e64 v73, |v64|, |v65|
	v_max3_f32 v77, v75, v72, v73
	v_pk_mul_f32 v[72:73], v[90:91], v[118:119] op_sel_hi:[1,0]
	v_pk_mul_f32 v[74:75], v[92:93], v[118:119] op_sel_hi:[1,0]
	v_pk_fma_f32 v[90:91], v[16:17], v[72:73], v[20:21]
	v_pk_fma_f32 v[84:85], v[18:19], v[74:75], v[22:23]
	v_pk_mul_f32 v[72:73], v[108:109], v[120:121] op_sel_hi:[1,0]
	v_pk_mul_f32 v[68:69], v[68:69], v[120:121] op_sel_hi:[1,0]
	v_pk_fma_f32 v[74:75], v[16:17], v[72:73], v[20:21]
	v_pk_fma_f32 v[68:69], v[18:19], v[68:69], v[22:23]
	v_max_f32_e64 v72, |v90|, |v91|
	v_max_f32_e64 v73, |v84|, |v85|
	v_max3_f32 v107, v76, v72, v73
	v_max_f32_e64 v72, |v74|, |v75|
	v_max_f32_e64 v73, |v68|, |v69|
	v_max3_f32 v108, v77, v72, v73
	v_pk_mul_f32 v[72:73], v[110:111], v[118:119] op_sel_hi:[1,0]
	v_pk_mul_f32 v[76:77], v[112:113], v[118:119] op_sel_hi:[1,0]
	v_pk_fma_f32 v[92:93], v[24:25], v[72:73], v[28:29]
	v_pk_fma_f32 v[88:89], v[26:27], v[76:77], v[30:31]
	v_pk_mul_f32 v[76:77], v[114:115], v[120:121] op_sel_hi:[1,0]
	v_pk_mul_f32 v[72:73], v[116:117], v[120:121] op_sel_hi:[1,0]
	v_pk_fma_f32 v[76:77], v[24:25], v[76:77], v[28:29]
	v_pk_fma_f32 v[72:73], v[26:27], v[72:73], v[30:31]
	v_max_f32_e64 v109, |v92|, |v93|
	v_max_f32_e64 v110, |v88|, |v89|
	v_max3_f32 v107, v107, v109, v110
	v_max_f32_e64 v109, |v76|, |v77|
	v_max_f32_e64 v110, |v72|, |v73|
	v_max3_f32 v108, v108, v109, v110
	v_mov_b32_dpp v109, v107 quad_perm:[1,0,3,2] row_mask:0xf bank_mask:0xf bound_ctrl:1
	v_max_f32_e32 v109, v109, v109
	v_max_f32_e32 v107, v107, v109
	s_andn2_b64 vcc, exec, s[10:11]
	s_nop 0
	v_mov_b32_dpp v109, v107 quad_perm:[2,3,0,1] row_mask:0xf bank_mask:0xf bound_ctrl:1
	v_max_f32_e32 v109, v109, v109
	v_max_f32_e32 v107, v107, v109
	s_nop 1
	v_mov_b32_dpp v109, v107 row_half_mirror row_mask:0xf bank_mask:0xf bound_ctrl:1
	v_max_f32_e32 v109, v109, v109
	v_max_f32_e32 v107, v107, v109
	s_nop 1
	v_mov_b32_dpp v109, v107 row_mirror row_mask:0xf bank_mask:0xf bound_ctrl:1
	v_max_f32_e32 v109, v109, v109
	v_max_f32_e32 v107, v107, v109
	s_nop 0
	v_readlane_b32 s12, v107, 0
	v_readlane_b32 s13, v107, 16
	v_readlane_b32 s15, v107, 32
	v_readlane_b32 s36, v107, 48
	v_mov_b32_dpp v107, v108 quad_perm:[1,0,3,2] row_mask:0xf bank_mask:0xf bound_ctrl:1
	v_max_f32_e32 v107, v107, v107
	v_max_f32_e32 v107, v108, v107
	s_nop 1
	v_mov_b32_dpp v108, v107 quad_perm:[2,3,0,1] row_mask:0xf bank_mask:0xf bound_ctrl:1
	v_max_f32_e32 v108, v108, v108
	v_max_f32_e32 v107, v107, v108
	s_nop 1
	v_mov_b32_dpp v108, v107 row_half_mirror row_mask:0xf bank_mask:0xf bound_ctrl:1
	v_max_f32_e32 v108, v108, v108
	v_max_f32_e32 v107, v107, v108
	s_nop 1
	v_mov_b32_dpp v108, v107 row_mirror row_mask:0xf bank_mask:0xf bound_ctrl:1
	v_max_f32_e32 v108, v108, v108
	v_max_f32_e32 v107, v107, v108
	s_nop 0
	v_readlane_b32 s37, v107, 0
	v_readlane_b32 s40, v107, 16
	v_readlane_b32 s41, v107, 32
	v_readlane_b32 s11, v107, 48
	s_cbranch_vccnz .LBB0_837
; __device__ __forceinline__ void p7_norm2(const Frame& F, int layer) {
;     ...
;         if (vR) { const float ia = ma > 0.f ? 127.f / ma : 0.f, ib = mb > 0.f ? 127.f / mb : 0.f;
; #pragma unroll
;           for (int j = 0; j < 4; ++j) { const int k = 4 * (lane + 64 * j);
;               const unsigned qa = pack_i8x4(va[j][0], va[j][1], va[j][2], va[j][3], ia), qb = pack_i8x4(vb[j][0], vb[j][1], vb[j][2], vb[j][3], ib);
;               *(unsigned*)(HQp + (size_t)rowA * D + k) = qa; *(unsigned*)(HQp + (size_t)rowB * D + k) = qb; }
;           if (lane == 0) { SAp[rowA] = ma * (1.f / 127.f); SAp[rowB] = mb * (1.f / 127.f); } }
	v_max_f32_e64 v107, s36, s36
	v_max_f32_e64 v110, s15, s15
	v_max_f32_e32 v107, v110, v107
	v_mov_b32_e32 v110, s13
	s_or_b32 s10, s3, 1
	v_max3_f32 v107, s12, v110, v107
	s_mov_b32 s3, 0x42fe0000
	v_div_scale_f32 v110, s[12:13], v107, v107, s3
	v_rcp_f32_e32 v111, v110
	v_max_f32_e64 v108, s11, s11
	v_max_f32_e64 v109, s41, s41
	v_max_f32_e32 v108, v109, v108
	v_mov_b32_e32 v109, s40
	v_max3_f32 v108, s37, v109, v108
	v_fma_f32 v109, -v110, v111, 1.0
	v_fmac_f32_e32 v111, v109, v111
	v_div_scale_f32 v109, vcc, s3, v107, s3
	v_mul_f32_e32 v112, v109, v111
	v_fma_f32 v113, -v110, v112, v109
	v_fmac_f32_e32 v112, v113, v111
	v_fma_f32 v109, -v110, v112, v109
	v_div_scale_f32 v110, s[12:13], v108, v108, s3
	v_div_fmas_f32 v109, v109, v111, v112
	v_rcp_f32_e32 v111, v110
	v_div_fixup_f32 v109, v109, v107, s3
	v_cmp_lt_f32_e32 vcc, 0, v107
	s_mov_b32 s15, 0xc0c0400
	v_fma_f32 v112, -v110, v111, 1.0
	v_cndmask_b32_e32 v109, 0, v109, vcc
	v_fmac_f32_e32 v111, v112, v111
	v_div_scale_f32 v112, vcc, s3, v108, s3
	v_mul_f32_e32 v113, v112, v111
	v_fma_f32 v114, -v110, v113, v112
	v_fmac_f32_e32 v113, v114, v111
	v_fma_f32 v110, -v110, v113, v112
	v_div_fmas_f32 v110, v110, v111, v113
	v_div_fixup_f32 v110, v110, v108, s3
	v_cmp_lt_f32_e32 vcc, 0, v108
	v_fmaak_f32 v111, v83, v109, 0x4b400000
	v_fmaak_f32 v112, v78, v109, 0x4b400000
	v_cndmask_b32_e32 v114, 0, v110, vcc
	v_fmaak_f32 v110, v82, v109, 0x4b400000
	v_fmaak_f32 v113, v79, v109, 0x4b400000
	v_perm_b32 v110, v111, v110, s15
	v_perm_b32 v111, v113, v112, s15
	s_mov_b32 s40, 0x5040100
	s_ashr_i32 s3, s2, 31
	v_perm_b32 v112, v111, v110, s40
	v_fmaak_f32 v110, v66, v114, 0x4b400000
	v_fmaak_f32 v111, v67, v114, 0x4b400000
	v_fmaak_f32 v113, v62, v114, 0x4b400000
	v_fmaak_f32 v115, v63, v114, 0x4b400000
	s_lshl_b64 s[12:13], s[2:3], 10
	s_ashr_i32 s11, s10, 31
	v_perm_b32 v110, v111, v110, s15
	v_perm_b32 v111, v115, v113, s15
	s_lshl_b64 s[36:37], s[10:11], 10
	v_perm_b32 v115, v111, v110, s40
	v_lshl_add_u64 v[110:111], v[34:35], 0, s[12:13]
	global_store_dword v[110:111], v112, off
	v_lshl_add_u64 v[112:113], v[34:35], 0, s[36:37]
	global_store_dword v[112:113], v115, off
	v_fmaak_f32 v115, v86, v109, 0x4b400000
	v_fmaak_f32 v116, v87, v109, 0x4b400000
	v_fmaak_f32 v117, v80, v109, 0x4b400000
	v_fmaak_f32 v118, v81, v109, 0x4b400000
	v_perm_b32 v115, v116, v115, s15
	v_perm_b32 v116, v118, v117, s15
	v_perm_b32 v115, v116, v115, s40
	v_fmaak_f32 v116, v70, v114, 0x4b400000
	v_fmaak_f32 v117, v71, v114, 0x4b400000
	v_fmaak_f32 v118, v64, v114, 0x4b400000
	v_fmaak_f32 v119, v65, v114, 0x4b400000
	v_perm_b32 v116, v117, v116, s15
	v_perm_b32 v117, v119, v118, s15
	v_perm_b32 v116, v117, v116, s40
	global_store_dword v[110:111], v115, off offset:256
	global_store_dword v[112:113], v116, off offset:256
	v_fmaak_f32 v115, v90, v109, 0x4b400000
	v_fmaak_f32 v116, v91, v109, 0x4b400000
	v_fmaak_f32 v117, v84, v109, 0x4b400000
	v_fmaak_f32 v118, v85, v109, 0x4b400000
	v_perm_b32 v115, v116, v115, s15
	v_perm_b32 v116, v118, v117, s15
	v_perm_b32 v115, v116, v115, s40
	v_fmaak_f32 v116, v74, v114, 0x4b400000
	v_fmaak_f32 v117, v75, v114, 0x4b400000
	v_fmaak_f32 v118, v68, v114, 0x4b400000
	v_fmaak_f32 v119, v69, v114, 0x4b400000
	v_perm_b32 v116, v117, v116, s15
	v_perm_b32 v117, v119, v118, s15
	v_perm_b32 v116, v117, v116, s40
	global_store_dword v[110:111], v115, off offset:512
	global_store_dword v[112:113], v116, off offset:512
	v_fmaak_f32 v115, v92, v109, 0x4b400000
	v_fmaak_f32 v116, v93, v109, 0x4b400000
	v_fmaak_f32 v117, v88, v109, 0x4b400000
	v_fmaak_f32 v109, v89, v109, 0x4b400000
	v_perm_b32 v115, v116, v115, s15
	v_perm_b32 v109, v109, v117, s15
	v_perm_b32 v109, v109, v115, s40
	v_fmaak_f32 v115, v76, v114, 0x4b400000
	v_fmaak_f32 v116, v77, v114, 0x4b400000
	v_fmaak_f32 v117, v72, v114, 0x4b400000
	v_fmaak_f32 v114, v73, v114, 0x4b400000
	v_perm_b32 v115, v116, v115, s15
	v_perm_b32 v114, v114, v117, s15
	v_perm_b32 v114, v114, v115, s40
	global_store_dword v[110:111], v109, off offset:768
	global_store_dword v[112:113], v114, off offset:768
	s_and_saveexec_b64 s[12:13], s[38:39]
	s_cbranch_execz .LBB0_836
	s_lshl_b64 s[36:37], s[2:3], 2
	s_add_u32 s36, s16, s36
	s_addc_u32 s37, s17, s37
	s_lshl_b64 s[10:11], s[10:11], 2
	v_mul_f32_e32 v107, 0x3c010204, v107
	s_add_u32 s10, s16, s10
	v_mul_f32_e32 v108, 0x3c010204, v108
	s_addc_u32 s11, s17, s11
	global_store_dword v145, v107, s[36:37]
	global_store_dword v145, v108, s[10:11]

; #define LAS __attribute__((address_space(3)))
; __device__ __forceinline__ unsigned pk2(float lo, float hi) { f32x2_t v = {lo, hi}; bf16x2_t b = __builtin_convertvector(v, bf16x2_t); return __builtin_bit_cast(unsigned, b); }
; __device__ __forceinline__ float bflo(unsigned w) { return __uint_as_float(w << 16); }
; __device__ __forceinline__ float bfhi(unsigned w) { return __uint_as_float(w & 0xffff0000u); }
; __device__ __forceinline__ void lds_barrier() { asm volatile("s_waitcnt lgkmcnt(0)" ::: "memory"); __builtin_amdgcn_s_barrier(); asm volatile("" ::: "memory"); }
; __device__ __forceinline__ void thin_stage_row(LAS unsigned char* L, int srow, const f32x4 (&h)[4], int lane) {
; #pragma unroll
;     for (int j = 0; j < 4; ++j) { const int k = 4 * (lane + 64 * j);
;         const u32x2 hi = {pk2(h[j][0], h[j][1]), pk2(h[j][2], h[j][3])};
;         const u32x2 lo = {pk2(h[j][0] - bflo(hi.x), h[j][1] - bfhi(hi.x)), pk2(h[j][2] - bflo(hi.y), h[j][3] - bfhi(hi.y))};
;         *(LAS u32x2*)(L + TH_HHI + srow * TH_STR + k * 2) = hi; *(LAS u32x2*)(L + TH_HLO + srow * TH_STR + k * 2) = lo; }
; }
; __device__ __forceinline__ void p7_norm2(const Frame& F, int layer) {
;     ...
;         thin_stage_row(F.lds, 2 * F.wave, va, lane); thin_stage_row(F.lds, 2 * F.wave + 1, vb, lane);
;         lds_barrier();
.LBB0_837:
	v_cvt_pk_bf16_f32 v108, v82, v83
	v_cvt_pk_bf16_f32 v109, v78, v79
	v_lshlrev_b32_e32 v110, 16, v108
	v_and_b32_e32 v111, 0xffff0000, v108
	v_pk_add_f32 v[82:83], v[82:83], v[110:111] neg_lo:[0,1] neg_hi:[0,1]
	v_lshlrev_b32_e32 v110, 16, v109
	v_and_b32_e32 v111, 0xffff0000, v109
	v_pk_add_f32 v[78:79], v[78:79], v[110:111] neg_lo:[0,1] neg_hi:[0,1]
	v_cvt_pk_bf16_f32 v82, v82, v83
	v_cvt_pk_bf16_f32 v83, v78, v79
	v_cvt_pk_bf16_f32 v78, v86, v87
	v_cvt_pk_bf16_f32 v79, v80, v81
	v_lshlrev_b32_e32 v110, 16, v78
	v_and_b32_e32 v111, 0xffff0000, v78
	v_pk_add_f32 v[86:87], v[86:87], v[110:111] neg_lo:[0,1] neg_hi:[0,1]
	v_lshlrev_b32_e32 v110, 16, v79
	v_and_b32_e32 v111, 0xffff0000, v79
	v_add_u32_e32 v107, s29, v94
	v_pk_add_f32 v[80:81], v[80:81], v[110:111] neg_lo:[0,1] neg_hi:[0,1]
	v_add_u32_e32 v112, s30, v94
	v_cvt_pk_bf16_f32 v86, v86, v87
	v_cvt_pk_bf16_f32 v87, v80, v81
	ds_write2st64_b64 v107, v[108:109], v[78:79] offset1:1
	ds_write2st64_b64 v112, v[82:83], v[86:87] offset1:1
	v_cvt_pk_bf16_f32 v78, v90, v91
	v_cvt_pk_bf16_f32 v79, v84, v85
	v_lshlrev_b32_e32 v80, 16, v78
	v_and_b32_e32 v81, 0xffff0000, v78
	v_lshlrev_b32_e32 v82, 16, v79
	v_and_b32_e32 v83, 0xffff0000, v79
	v_pk_add_f32 v[80:81], v[90:91], v[80:81] neg_lo:[0,1] neg_hi:[0,1]
	v_pk_add_f32 v[82:83], v[84:85], v[82:83] neg_lo:[0,1] neg_hi:[0,1]
	v_cvt_pk_bf16_f32 v80, v80, v81
	v_cvt_pk_bf16_f32 v81, v82, v83
	v_cvt_pk_bf16_f32 v82, v92, v93
	v_cvt_pk_bf16_f32 v83, v88, v89
	v_lshlrev_b32_e32 v84, 16, v82
	v_and_b32_e32 v85, 0xffff0000, v82
	v_lshlrev_b32_e32 v86, 16, v83
	v_and_b32_e32 v87, 0xffff0000, v83
	v_pk_add_f32 v[84:85], v[92:93], v[84:85] neg_lo:[0,1] neg_hi:[0,1]
	v_pk_add_f32 v[86:87], v[88:89], v[86:87] neg_lo:[0,1] neg_hi:[0,1]
	v_cvt_pk_bf16_f32 v84, v84, v85
	v_cvt_pk_bf16_f32 v85, v86, v87
	ds_write2st64_b64 v107, v[78:79], v[82:83] offset0:2 offset1:3
	ds_write2st64_b64 v112, v[80:81], v[84:85] offset0:2 offset1:3
	v_cvt_pk_bf16_f32 v78, v66, v67
	v_cvt_pk_bf16_f32 v79, v62, v63
	v_lshlrev_b32_e32 v80, 16, v78
	v_and_b32_e32 v81, 0xffff0000, v78
	v_pk_add_f32 v[66:67], v[66:67], v[80:81] neg_lo:[0,1] neg_hi:[0,1]
	v_lshlrev_b32_e32 v80, 16, v79
	v_and_b32_e32 v81, 0xffff0000, v79
	v_pk_add_f32 v[62:63], v[62:63], v[80:81] neg_lo:[0,1] neg_hi:[0,1]
	v_cvt_pk_bf16_f32 v66, v66, v67
	v_cvt_pk_bf16_f32 v67, v62, v63
	v_cvt_pk_bf16_f32 v62, v70, v71
	ds_write_b64 v103, v[78:79]
	ds_write_b64 v104, v[66:67]
	v_cvt_pk_bf16_f32 v63, v64, v65
	v_lshlrev_b32_e32 v66, 16, v62
	v_and_b32_e32 v67, 0xffff0000, v62
	v_pk_add_f32 v[66:67], v[70:71], v[66:67] neg_lo:[0,1] neg_hi:[0,1]
	v_lshlrev_b32_e32 v70, 16, v63
	v_and_b32_e32 v71, 0xffff0000, v63
	v_pk_add_f32 v[64:65], v[64:65], v[70:71] neg_lo:[0,1] neg_hi:[0,1]
	v_cvt_pk_bf16_f32 v66, v66, v67
	v_cvt_pk_bf16_f32 v67, v64, v65
	v_cvt_pk_bf16_f32 v64, v74, v75
	v_cvt_pk_bf16_f32 v65, v68, v69
	v_lshlrev_b32_e32 v70, 16, v64
	v_and_b32_e32 v71, 0xffff0000, v64
	v_pk_add_f32 v[70:71], v[74:75], v[70:71] neg_lo:[0,1] neg_hi:[0,1]
	v_lshlrev_b32_e32 v74, 16, v65
	v_and_b32_e32 v75, 0xffff0000, v65
	v_add_u32_e32 v78, s34, v94
	v_pk_add_f32 v[68:69], v[68:69], v[74:75] neg_lo:[0,1] neg_hi:[0,1]
	v_add_u32_e32 v79, s35, v94
	v_cvt_pk_bf16_f32 v70, v70, v71
	v_cvt_pk_bf16_f32 v71, v68, v69
	ds_write2st64_b64 v78, v[62:63], v[64:65] offset0:1 offset1:2
	ds_write2st64_b64 v79, v[66:67], v[70:71] offset0:1 offset1:2
	v_cvt_pk_bf16_f32 v62, v76, v77
	v_cvt_pk_bf16_f32 v63, v72, v73
	v_lshlrev_b32_e32 v64, 16, v62
	v_and_b32_e32 v65, 0xffff0000, v62
	v_lshlrev_b32_e32 v66, 16, v63
	v_and_b32_e32 v67, 0xffff0000, v63
	v_pk_add_f32 v[64:65], v[76:77], v[64:65] neg_lo:[0,1] neg_hi:[0,1]
	v_pk_add_f32 v[66:67], v[72:73], v[66:67] neg_lo:[0,1] neg_hi:[0,1]
	v_cvt_pk_bf16_f32 v64, v64, v65
	v_cvt_pk_bf16_f32 v65, v66, v67
	ds_write_b64 v78, v[62:63] offset:1536
	ds_write_b64 v79, v[64:65] offset:1536
	s_waitcnt lgkmcnt(0)
	s_barrier
; #define LAS __attribute__((address_space(3)))
; __device__ __forceinline__ float shx(float v, int m, int lane) { return __int_as_float(__builtin_amdgcn_ds_bpermute((lane ^ m) << 2, __float_as_int(v))); }
; __device__ __forceinline__ void lds_barrier() { asm volatile("s_waitcnt lgkmcnt(0)" ::: "memory"); __builtin_amdgcn_s_barrier(); asm volatile("" ::: "memory"); }
; __device__ __forceinline__ void thin_mfma_partial(LAS unsigned char* L, int wave, int lane) {
;     const int fr = lane & 15, fq = lane >> 4;
;     f32x4 acc = {0.f, 0.f, 0.f, 0.f};
; #pragma unroll
;     for (int s = 0; s < 4; ++s) { const int off = fr * TH_STR + (32 * (4 * wave + s) + 8 * fq) * 2;
;         const bf16x8 ahi = *(LAS const bf16x8*)(L + TH_HHI + off), alo = *(LAS const bf16x8*)(L + TH_HLO + off);
;         const bf16x8 bhi = *(LAS const bf16x8*)(L + TH_THI + off), blo = *(LAS const bf16x8*)(L + TH_TLO + off);
;         acc = __builtin_amdgcn_mfma_f32_16x16x32_bf16(ahi, bhi, acc, 0, 0, 0);
;         acc = __builtin_amdgcn_mfma_f32_16x16x32_bf16(ahi, blo, acc, 0, 0, 0);
;         acc = __builtin_amdgcn_mfma_f32_16x16x32_bf16(alo, bhi, acc, 0, 0, 0); }
;     LAS float* P = (LAS float*)(L + TH_PART) + wave * 256;
; #pragma unroll
;     for (int t2 = 0; t2 < 4; ++t2) P[(4 * fq + t2) * 16 + fr] = acc[t2];
; }
; __device__ __forceinline__ void p7_norm2(const Frame& F, int layer) {
;     ...
;         thin_mfma_partial(F.lds, F.wave, lane);
;         lds_barrier();
;         if (F.wave < 4) { const int t16 = F.wave * 64 + lane, srow = t16 >> 4, c = t16 & 15; const float lg = thin_total(F.lds, t16);
;             float mx = lg;
; #pragma unroll
;             for (int o = 1; o < 16; o <<= 1) mx = fmaxf(mx, shx(mx, o, lane));
;             const float ex = __expf(lg - mx); float se = ex;
; #pragma unroll
;             for (int o = 1; o < 16; o <<= 1) se += shx(se, o, lane);
;             const int row = (F.blk * NWAVES + (srow >> 1)) * RW + 2 * pi + (srow & 1);
;             if (row < nrows) { const float a = ex / se;
;                 if (row < NL) AFFp[((size_t)((row >> 11) * 16 + c)) * 2048 + (row & 2047)] = a;
;                 else { const int r = row - NL; AFFp[(size_t)NL * 16 + ((size_t)((r >> 8) * 16 + c)) * 256 + (r & 255)] = a; } } }
	v_add_u32_e32 v90, 0x10200, v106
	ds_read_b128 v[62:65], v90
	ds_read_b128 v[66:69], v106
	ds_read_b128 v[70:73], v90 offset:64
	ds_read_b128 v[74:77], v106 offset:64
	ds_read_b128 v[82:85], v106 offset:33024
	ds_read_b128 v[86:89], v106 offset:33088
	s_waitcnt lgkmcnt(4)
	v_mfma_f32_16x16x32_bf16 v[78:81], v[62:65], v[66:69], 0
	v_add_u32_e32 v91, 0x18300, v106
	s_andn2_b64 vcc, exec, s[6:7]
	s_waitcnt lgkmcnt(1)
	v_mfma_f32_16x16x32_bf16 v[62:65], v[62:65], v[82:85], v[78:81]
	s_nop 3
	ds_read_b128 v[78:81], v91
	ds_read_b128 v[82:85], v91 offset:64
	s_waitcnt lgkmcnt(1)
	v_mfma_f32_16x16x32_bf16 v[62:65], v[78:81], v[66:69], v[62:65]
	ds_read_b128 v[66:69], v90 offset:128
	v_mfma_f32_16x16x32_bf16 v[62:65], v[70:73], v[74:77], v[62:65]
	v_mfma_f32_16x16x32_bf16 v[62:65], v[70:73], v[86:89], v[62:65]
	s_waitcnt lgkmcnt(1)
	v_mfma_f32_16x16x32_bf16 v[62:65], v[82:85], v[74:77], v[62:65]
	ds_read_b128 v[70:73], v106 offset:128
	ds_read_b128 v[74:77], v90 offset:192
	ds_read_b128 v[78:81], v106 offset:192
	ds_read_b128 v[82:85], v106 offset:33152
	ds_read_b128 v[86:89], v106 offset:33216
	s_waitcnt lgkmcnt(4)
	v_mfma_f32_16x16x32_bf16 v[62:65], v[66:69], v[70:73], v[62:65]
	s_waitcnt lgkmcnt(1)
	v_mfma_f32_16x16x32_bf16 v[62:65], v[66:69], v[82:85], v[62:65]
	ds_read_b128 v[66:69], v91 offset:128
	ds_read_b128 v[82:85], v91 offset:192
	s_waitcnt lgkmcnt(1)
	v_mfma_f32_16x16x32_bf16 v[62:65], v[66:69], v[70:73], v[62:65]
	v_mfma_f32_16x16x32_bf16 v[62:65], v[74:77], v[78:81], v[62:65]
	v_mfma_f32_16x16x32_bf16 v[62:65], v[74:77], v[86:89], v[62:65]
	s_waitcnt lgkmcnt(0)
	v_mfma_f32_16x16x32_bf16 v[62:65], v[82:85], v[78:81], v[62:65]
	s_nop 7
	ds_write2_b32 v105, v62, v63 offset1:16
	ds_write2_b32 v105, v64, v65 offset0:32 offset1:48
	s_waitcnt vmcnt(0)
	s_waitcnt lgkmcnt(0)
	s_barrier
	s_cbranch_vccnz .LBB0_828
	ds_read2st64_b32 v[62:63], v97 offset1:4
	s_waitcnt lgkmcnt(0)
	v_add_f32_e32 v62, 0, v62
	v_add_f32_e32 v64, v62, v63
	ds_read2st64_b32 v[62:63], v97 offset0:8 offset1:12
	s_waitcnt lgkmcnt(0)
	v_add_f32_e32 v62, v64, v62
	v_add_f32_e32 v64, v62, v63
	ds_read2st64_b32 v[62:63], v97 offset0:16 offset1:20
	s_waitcnt lgkmcnt(0)
	v_add_f32_e32 v62, v64, v62
	v_add_f32_e32 v64, v62, v63
	ds_read2st64_b32 v[62:63], v97 offset0:24 offset1:28
	s_waitcnt lgkmcnt(0)
	v_add_f32_e32 v62, v64, v62
	v_add_f32_e32 v62, v62, v63
	ds_bpermute_b32 v63, v98, v62
	s_waitcnt lgkmcnt(0)
	v_max_f32_e32 v63, v63, v63
	v_max_f32_e32 v63, v62, v63
	ds_bpermute_b32 v64, v99, v63
	s_waitcnt lgkmcnt(0)
	v_max_f32_e32 v64, v64, v64
	v_max_f32_e32 v63, v63, v64
	ds_bpermute_b32 v64, v100, v63
	s_waitcnt lgkmcnt(0)
	v_max_f32_e32 v64, v64, v64
	v_max_f32_e32 v63, v63, v64
	ds_bpermute_b32 v64, v101, v63
	s_waitcnt lgkmcnt(0)
	v_max_f32_e32 v64, v64, v64
	v_max_f32_e32 v63, v63, v64
	v_sub_f32_e32 v62, v62, v63
	v_mul_f32_e32 v62, 0x3fb8aa3b, v62
	v_exp_f32_e32 v63, v62
	ds_bpermute_b32 v62, v98, v63
	s_waitcnt lgkmcnt(0)
	v_add_f32_e32 v62, v63, v62
	ds_bpermute_b32 v64, v99, v62
	s_waitcnt lgkmcnt(0)
	v_add_f32_e32 v62, v62, v64
	ds_bpermute_b32 v64, v100, v62
	s_waitcnt lgkmcnt(0)
	v_add_f32_e32 v64, v62, v64
	ds_bpermute_b32 v65, v101, v64
	v_add_u32_e32 v62, v96, v102
	v_cmp_gt_i32_e32 vcc, s18, v62
	s_and_saveexec_b64 s[10:11], vcc
	s_cbranch_execz .LBB0_827
	s_waitcnt lgkmcnt(0)
	v_add_f32_e32 v64, v64, v65
	v_div_scale_f32 v65, s[12:13], v64, v64, v63
	v_rcp_f32_e32 v66, v65
	v_div_scale_f32 v67, vcc, v63, v64, v63
	s_movk_i32 s3, 0x7fff
	v_fma_f32 v68, -v65, v66, 1.0
	v_fmac_f32_e32 v66, v68, v66
	v_mul_f32_e32 v68, v67, v66
	v_fma_f32 v69, -v65, v68, v67
	v_fmac_f32_e32 v68, v69, v66
	v_fma_f32 v65, -v65, v68, v67
	v_div_fmas_f32 v65, v65, v66, v68
	v_div_fixup_f32 v63, v65, v64, v63
	v_cmp_lt_i32_e32 vcc, s3, v62
	s_and_saveexec_b64 s[12:13], vcc
	s_xor_b64 s[12:13], exec, s[12:13]
	s_cbranch_execz .LBB0_841
	v_add_u32_e32 v64, 0xffff8000, v102
	v_lshrrev_b32_e32 v64, 4, v64
	s_mov_b32 s3, 0xffffff0
	v_and_or_b32 v144, v64, s3, v95
	v_lshlrev_b64 v[64:65], 10, v[144:145]
	v_mov_b32_e32 v66, 2
	v_lshl_add_u64 v[64:65], s[4:5], 0, v[64:65]
	v_lshlrev_b32_sdwa v144, v66, v62 dst_sel:DWORD dst_unused:UNUSED_PAD src0_sel:DWORD src1_sel:BYTE_0
	v_lshl_add_u64 v[64:65], v[64:65], 0, v[144:145]
	v_add_co_u32_e32 v64, vcc, 0x200000, v64
	s_nop 1
	v_addc_co_u32_e32 v65, vcc, 0, v65, vcc
	global_store_dword v[64:65], v63, off
